# P6 logits loop requests the second half of the H columns during the first pass (cache warm-up loads)
# baseline (speedup 1.0000x reference)
; __device__ __forceinline__ float bf_lo(unsigned u) { return __uint_as_float(u << 16); }
; __device__ __forceinline__ float bf_hi(unsigned u) { return __uint_as_float(u & 0xffff0000u); }
; __device__ __forceinline__ f32x4 mma16(bf16x8 xrow, bf16x8 ycol, f32x4 c) { return __builtin_amdgcn_mfma_f32_16x16x32_bf16(xrow, ycol, c, 0, 0, 0); }
; __device__ __forceinline__ void p6_router(Ctx& X) {
;     ...
; #pragma unroll 4
;         for (int ks = 0; ks < 8; ++ks) { const int kb = 256 * w + 32 * ks + 8 * fq;
;             bf16x8 ah[2], bh[2], bl[2];
; #pragma unroll
;             for (int mt = 0; mt < 2; ++mt) { const u32x4 hv = *(const u32x4*)(XP_Hh(X) + (size_t)(tb + 16 * mt + fr) * D + kb);
;                 const float f0 = bf_lo(hv.x), f1 = bf_hi(hv.x), f2 = bf_lo(hv.y), f3 = bf_hi(hv.y), f4 = bf_lo(hv.z), f5 = bf_hi(hv.z), f6 = bf_lo(hv.w), f7 = bf_hi(hv.w);
;                 ss[mt] += (f0 * f0 + f1 * f1) + (f2 * f2 + f3 * f3) + (f4 * f4 + f5 * f5) + (f6 * f6 + f7 * f7);
;                 ah[mt] = __builtin_bit_cast(bf16x8, hv); }
; #pragma unroll
;             for (int nt = 0; nt < 2; ++nt) { bh[nt] = *(const bf16x8*)(XP_WRH(X) + (size_t)(16 * nt + fr) * D + kb); bl[nt] = *(const bf16x8*)(XP_WRL(X) + (size_t)(16 * nt + fr) * D + kb); }
; #pragma unroll
;             for (int mt = 0; mt < 2; ++mt)
; #pragma unroll
;                 for (int nt = 0; nt < 2; ++nt) { acc[mt][nt] = mma16(bh[nt], ah[mt], acc[mt][nt]); acc[mt][nt] = mma16(bl[nt], ah[mt], acc[mt][nt]); }
;         }
.LBB0_817:
	v_add_u32_e32 v24, s8, v110
	v_ashrrev_i32_e32 v25, 31, v24
	v_add_u32_e32 v26, 32, v24
	v_add_u32_e32 v28, 64, v24
	v_add_u32_e32 v30, 0x60, v24
	v_lshlrev_b64 v[24:25], 1, v[24:25]
	v_ashrrev_i32_e32 v27, 31, v26
	v_ashrrev_i32_e32 v29, 31, v28
	v_ashrrev_i32_e32 v31, 31, v30
	v_lshl_add_u64 v[32:33], s[26:27], 0, v[24:25]
	v_lshl_add_u64 v[34:35], s[28:29], 0, v[24:25]
	v_lshl_add_u64 v[24:25], s[30:31], 0, v[24:25]
	v_lshlrev_b64 v[26:27], 1, v[26:27]
	v_lshlrev_b64 v[28:29], 1, v[28:29]
	v_lshlrev_b64 v[30:31], 1, v[30:31]
	v_lshl_add_u64 v[36:37], v[32:33], 0, v[18:19]
	v_lshl_add_u64 v[32:33], v[32:33], 0, v[20:21]
	v_lshl_add_u64 v[60:61], v[34:35], 0, v[56:57]
	v_lshl_add_u64 v[62:63], v[24:25], 0, v[56:57]
	v_lshl_add_u64 v[64:65], v[34:35], 0, v[58:59]
	v_lshl_add_u64 v[68:69], v[24:25], 0, v[58:59]
	v_lshl_add_u64 v[72:73], s[26:27], 0, v[26:27]
	v_lshl_add_u64 v[74:75], s[28:29], 0, v[26:27]
	v_lshl_add_u64 v[76:77], s[30:31], 0, v[26:27]
	v_lshl_add_u64 v[78:79], s[26:27], 0, v[28:29]
	v_lshl_add_u64 v[80:81], s[28:29], 0, v[28:29]
	v_lshl_add_u64 v[82:83], s[30:31], 0, v[28:29]
	v_lshl_add_u64 v[84:85], s[26:27], 0, v[30:31]
	v_lshl_add_u64 v[86:87], s[28:29], 0, v[30:31]
	v_lshl_add_u64 v[88:89], s[30:31], 0, v[30:31]
	global_load_dwordx4 v[24:27], v[36:37], off
	global_load_dwordx4 v[244:247], v[36:37], off offset:256
	global_load_dwordx4 v[28:31], v[32:33], off
	global_load_dwordx4 v[244:247], v[32:33], off offset:256
	s_nop 0
	global_load_dwordx4 v[32:35], v[60:61], off
	s_nop 0
	global_load_dwordx4 v[60:63], v[62:63], off
	s_nop 0
	global_load_dwordx4 v[64:67], v[64:65], off
	s_nop 0
	global_load_dwordx4 v[68:71], v[68:69], off
	v_lshl_add_u64 v[36:37], v[72:73], 0, v[18:19]
	v_lshl_add_u64 v[90:91], v[72:73], 0, v[20:21]
	v_lshl_add_u64 v[96:97], v[74:75], 0, v[56:57]
	v_lshl_add_u64 v[100:101], v[76:77], 0, v[56:57]
	v_lshl_add_u64 v[126:127], v[74:75], 0, v[58:59]
	v_lshl_add_u64 v[130:131], v[76:77], 0, v[58:59]
	v_lshl_add_u64 v[92:93], v[78:79], 0, v[18:19]
	v_lshl_add_u64 v[94:95], v[78:79], 0, v[20:21]
	v_lshl_add_u64 v[134:135], v[80:81], 0, v[56:57]
	v_lshl_add_u64 v[138:139], v[82:83], 0, v[56:57]
	v_lshl_add_u64 v[142:143], v[80:81], 0, v[58:59]
	v_lshl_add_u64 v[146:147], v[82:83], 0, v[58:59]
	v_lshl_add_u64 v[98:99], v[84:85], 0, v[18:19]
	v_lshl_add_u64 v[102:103], v[84:85], 0, v[20:21]
	v_lshl_add_u64 v[150:151], v[86:87], 0, v[56:57]
	v_lshl_add_u64 v[154:155], v[88:89], 0, v[56:57]
	v_lshl_add_u64 v[158:159], v[86:87], 0, v[58:59]
	v_lshl_add_u64 v[162:163], v[88:89], 0, v[58:59]
	global_load_dwordx4 v[72:75], v[36:37], off
	global_load_dwordx4 v[244:247], v[36:37], off offset:256
	global_load_dwordx4 v[76:79], v[90:91], off
	global_load_dwordx4 v[244:247], v[90:91], off offset:256
	global_load_dwordx4 v[80:83], v[92:93], off
	global_load_dwordx4 v[244:247], v[92:93], off offset:256
	global_load_dwordx4 v[84:87], v[94:95], off
	global_load_dwordx4 v[244:247], v[94:95], off offset:256
	s_nop 0
	global_load_dwordx4 v[88:91], v[98:99], off
	global_load_dwordx4 v[244:247], v[98:99], off offset:256
	global_load_dwordx4 v[92:95], v[102:103], off
	global_load_dwordx4 v[244:247], v[102:103], off offset:256
	s_nop 0
	global_load_dwordx4 v[96:99], v[96:97], off
	s_nop 0
	global_load_dwordx4 v[100:103], v[100:101], off
	s_nop 0
	global_load_dwordx4 v[126:129], v[126:127], off
	s_nop 0
	global_load_dwordx4 v[130:133], v[130:131], off
	s_nop 0
	global_load_dwordx4 v[134:137], v[134:135], off
	s_nop 0
	global_load_dwordx4 v[138:141], v[138:139], off
	s_nop 0
	global_load_dwordx4 v[142:145], v[142:143], off
	s_nop 0
	global_load_dwordx4 v[146:149], v[146:147], off
	s_nop 0
	global_load_dwordx4 v[150:153], v[150:151], off
	s_nop 0
	global_load_dwordx4 v[154:157], v[154:155], off
	s_nop 0
	global_load_dwordx4 v[158:161], v[158:159], off
	s_nop 0
	global_load_dwordx4 v[162:165], v[162:163], off
	s_addk_i32 s8, 0x80
	s_cmpk_eq_i32 s8, 0x100
	s_waitcnt vmcnt(27)
	v_mfma_f32_16x16x32_bf16 v[10:13], v[32:35], v[24:27], v[10:13]
	v_and_b32_e32 v167, 0xffff0000, v25
	v_and_b32_e32 v37, 0xffff0000, v24
	v_and_b32_e32 v171, 0xffff0000, v27
	s_waitcnt vmcnt(25)
	v_mfma_f32_16x16x32_bf16 v[14:17], v[64:67], v[24:27], v[14:17]
	v_and_b32_e32 v169, 0xffff0000, v26
	v_and_b32_e32 v175, 0xffff0000, v29
	v_and_b32_e32 v174, 0xffff0000, v28
	v_mfma_f32_16x16x32_bf16 v[2:5], v[32:35], v[28:31], v[2:5]
	v_and_b32_e32 v179, 0xffff0000, v31
	v_and_b32_e32 v178, 0xffff0000, v30
	v_lshlrev_b32_e32 v36, 16, v24
	v_mfma_f32_16x16x32_bf16 v[6:9], v[64:67], v[28:31], v[6:9]
	v_lshlrev_b32_e32 v166, 16, v25
	v_lshlrev_b32_e32 v168, 16, v26
	v_lshlrev_b32_e32 v170, 16, v27
	v_mfma_f32_16x16x32_bf16 v[10:13], v[60:63], v[24:27], v[10:13]
	v_lshlrev_b32_e32 v173, 16, v29
	v_lshlrev_b32_e32 v172, 16, v28
	v_lshlrev_b32_e32 v177, 16, v31
	s_waitcnt vmcnt(24)
	v_mfma_f32_16x16x32_bf16 v[14:17], v[68:71], v[24:27], v[14:17]
	v_lshlrev_b32_e32 v176, 16, v30
	v_mul_f32_e32 v38, v37, v37
	v_mul_f32_e32 v180, v167, v167
	v_mfma_f32_16x16x32_bf16 v[2:5], v[60:63], v[28:31], v[2:5]
	v_mul_f32_e32 v182, v169, v169
	v_mul_f32_e32 v184, v171, v171
	v_pk_mul_f32 v[174:175], v[174:175], v[174:175]
	v_mfma_f32_16x16x32_bf16 v[6:9], v[68:71], v[28:31], v[6:9]
	v_mul_f32_e64 v178, v178, v178
	v_mul_f32_e64 v179, v179, v179
	s_waitcnt vmcnt(23)
	v_and_b32_e32 v187, 0xffff0000, v72
	v_and_b32_e32 v189, 0xffff0000, v73
	s_waitcnt vmcnt(11)
	v_mfma_f32_16x16x32_bf16 v[10:13], v[96:99], v[72:75], v[10:13]
	v_and_b32_e32 v191, 0xffff0000, v74
	v_and_b32_e32 v199, 0xffff0000, v77
	v_and_b32_e32 v198, 0xffff0000, v76
	s_waitcnt vmcnt(9)
; __device__ __forceinline__ float bf_lo(unsigned u) { return __uint_as_float(u << 16); }
; __device__ __forceinline__ float bf_hi(unsigned u) { return __uint_as_float(u & 0xffff0000u); }
; __device__ __forceinline__ f32x4 mma16(bf16x8 xrow, bf16x8 ycol, f32x4 c) { return __builtin_amdgcn_mfma_f32_16x16x32_bf16(xrow, ycol, c, 0, 0, 0); }
; __device__ __forceinline__ void p6_router(Ctx& X) {
;     ...
;             for (int mt = 0; mt < 2; ++mt) { const u32x4 hv = *(const u32x4*)(XP_Hh(X) + (size_t)(tb + 16 * mt + fr) * D + kb);
;                 const float f0 = bf_lo(hv.x), f1 = bf_hi(hv.x), f2 = bf_lo(hv.y), f3 = bf_hi(hv.y), f4 = bf_lo(hv.z), f5 = bf_hi(hv.z), f6 = bf_lo(hv.w), f7 = bf_hi(hv.w);
;                 ss[mt] += (f0 * f0 + f1 * f1) + (f2 * f2 + f3 * f3) + (f4 * f4 + f5 * f5) + (f6 * f6 + f7 * f7);
;                 ah[mt] = __builtin_bit_cast(bf16x8, hv); }
; #pragma unroll
;             for (int nt = 0; nt < 2; ++nt) { bh[nt] = *(const bf16x8*)(XP_WRH(X) + (size_t)(16 * nt + fr) * D + kb); bl[nt] = *(const bf16x8*)(XP_WRL(X) + (size_t)(16 * nt + fr) * D + kb); }
; #pragma unroll
;             for (int mt = 0; mt < 2; ++mt)
; #pragma unroll
;                 for (int nt = 0; nt < 2; ++nt) { acc[mt][nt] = mma16(bh[nt], ah[mt], acc[mt][nt]); acc[mt][nt] = mma16(bl[nt], ah[mt], acc[mt][nt]); }
;         }
; #pragma unroll
;         for (int mt = 0; mt < 2; ++mt) { float q = ss[mt]; q += __shfl_xor(q, 16); q += __shfl_xor(q, 32); if (fq == 0) ssq[w * 32 + 16 * mt + fr] = q;
	v_mfma_f32_16x16x32_bf16 v[14:17], v[126:129], v[72:75], v[14:17]
	v_lshlrev_b32_e32 v186, 16, v72
	v_lshlrev_b32_e32 v188, 16, v73
	v_lshlrev_b32_e32 v190, 16, v74
	v_mfma_f32_16x16x32_bf16 v[2:5], v[96:99], v[76:79], v[2:5]
	v_and_b32_e32 v193, 0xffff0000, v75
	v_lshlrev_b32_e32 v197, 16, v77
	v_lshlrev_b32_e32 v196, 16, v76
	v_mfma_f32_16x16x32_bf16 v[6:9], v[126:129], v[76:79], v[6:9]
	v_and_b32_e32 v203, 0xffff0000, v79
	v_and_b32_e32 v202, 0xffff0000, v78
	v_and_b32_e32 v207, 0xffff0000, v81
	v_mfma_f32_16x16x32_bf16 v[10:13], v[100:103], v[72:75], v[10:13]
	v_and_b32_e32 v205, 0xffff0000, v80
	v_and_b32_e32 v215, 0xffff0000, v85
	v_and_b32_e32 v214, 0xffff0000, v84
	s_waitcnt vmcnt(8)
	v_mfma_f32_16x16x32_bf16 v[14:17], v[130:133], v[72:75], v[14:17]
	v_and_b32_e32 v33, 0xffff0000, v88
	v_and_b32_e32 v35, 0xffff0000, v89
	v_and_b32_e32 v65, 0xffff0000, v90
	v_mfma_f32_16x16x32_bf16 v[2:5], v[100:103], v[76:79], v[2:5]
	v_and_b32_e32 v67, 0xffff0000, v91
	v_and_b32_e32 v25, 0xffff0000, v93
	v_and_b32_e32 v24, 0xffff0000, v92
	v_mfma_f32_16x16x32_bf16 v[6:9], v[130:133], v[76:79], v[6:9]
	v_and_b32_e32 v61, 0xffff0000, v95
	v_and_b32_e32 v60, 0xffff0000, v94
	v_pk_fma_f32 v[28:29], v[36:37], v[36:37], v[38:39] op_sel_hi:[1,1,0]
	s_waitcnt vmcnt(7)
	v_mfma_f32_16x16x32_bf16 v[10:13], v[134:137], v[80:83], v[10:13]
	v_fma_f32 v30, v166, v166, v180
	v_fma_f32 v31, v167, v167, v180
	v_pk_fma_f32 v[36:37], v[168:169], v[168:169], v[182:183] op_sel_hi:[1,1,0]
	v_pk_fma_f32 v[62:63], v[170:171], v[170:171], v[184:185] op_sel_hi:[1,1,0]
	s_waitcnt vmcnt(5)
	v_mfma_f32_16x16x32_bf16 v[14:17], v[142:145], v[80:83], v[14:17]
	v_fma_f32 v68, v172, v172, v174
	v_fma_f32 v69, v173, v173, v175
	v_pk_fma_f32 v[70:71], v[176:177], v[176:177], v[178:179]
	v_mul_f32_e32 v38, v187, v187
	v_mfma_f32_16x16x32_bf16 v[2:5], v[134:137], v[84:87], v[2:5]
	v_mul_f32_e32 v166, v189, v189
	v_mul_f32_e32 v96, v191, v191
	v_pk_mul_f32 v[168:169], v[198:199], v[198:199]
	v_mfma_f32_16x16x32_bf16 v[6:9], v[142:145], v[84:87], v[6:9]
	v_lshlrev_b32_e32 v192, 16, v75
	v_lshlrev_b32_e32 v201, 16, v79
	v_lshlrev_b32_e32 v200, 16, v78
	v_mfma_f32_16x16x32_bf16 v[10:13], v[138:141], v[80:83], v[10:13]
	v_lshlrev_b32_e32 v204, 16, v80
	v_lshlrev_b32_e32 v206, 16, v81
	v_and_b32_e32 v209, 0xffff0000, v82
	s_waitcnt vmcnt(4)
	v_mfma_f32_16x16x32_bf16 v[14:17], v[146:149], v[80:83], v[14:17]
	v_lshlrev_b32_e32 v213, 16, v85
	v_lshlrev_b32_e32 v212, 16, v84
	v_and_b32_e32 v219, 0xffff0000, v87
	v_mfma_f32_16x16x32_bf16 v[2:5], v[138:141], v[84:87], v[2:5]
	v_and_b32_e32 v218, 0xffff0000, v86
	v_lshlrev_b32_e32 v32, 16, v88
	v_lshlrev_b32_e32 v34, 16, v89
	v_mfma_f32_16x16x32_bf16 v[6:9], v[146:149], v[84:87], v[6:9]
	v_lshlrev_b32_e32 v64, 16, v90
	v_lshlrev_b32_e32 v66, 16, v91
	v_lshlrev_b32_e32 v221, 16, v93
	v_lshlrev_b32_e32 v220, 16, v92
	v_lshlrev_b32_e32 v27, 16, v95
	v_lshlrev_b32_e32 v26, 16, v94
	v_mul_f32_e32 v98, v193, v193
	v_pk_mul_f32 v[126:127], v[202:203], v[202:203]
	v_mul_f32_e32 v128, v205, v205
	v_mul_f32_e32 v170, v207, v207
	v_pk_mul_f32 v[176:177], v[214:215], v[214:215]
	v_mul_f32_e32 v74, v33, v33
	v_mul_f32_e32 v178, v35, v35
	v_mul_f32_e32 v100, v65, v65
	v_mul_f32_e32 v102, v67, v67
	v_pk_mul_f32 v[24:25], v[24:25], v[24:25]
	v_pk_mul_f32 v[60:61], v[60:61], v[60:61]
	v_mov_b32_e32 v29, v68
	v_mov_b32_e32 v31, v69
	v_mov_b32_e32 v37, v70
	v_mov_b32_e32 v63, v71
	v_pk_fma_f32 v[68:69], v[186:187], v[186:187], v[38:39] op_sel_hi:[1,1,0]
	v_pk_fma_f32 v[70:71], v[188:189], v[188:189], v[166:167] op_sel_hi:[1,1,0]
	v_pk_fma_f32 v[76:77], v[190:191], v[190:191], v[96:97] op_sel_hi:[1,1,0]
	v_pk_fma_f32 v[96:97], v[196:197], v[196:197], v[168:169]
	s_waitcnt vmcnt(3)
	v_mfma_f32_16x16x32_bf16 v[10:13], v[150:153], v[88:91], v[10:13]
	v_lshlrev_b32_e32 v208, 16, v82
	v_and_b32_e32 v211, 0xffff0000, v83
	v_lshlrev_b32_e32 v217, 16, v87
	s_waitcnt vmcnt(1)
	v_mfma_f32_16x16x32_bf16 v[14:17], v[158:161], v[88:91], v[14:17]
	v_lshlrev_b32_e32 v216, 16, v86
	v_mul_f32_e32 v172, v209, v209
	v_pk_mul_f32 v[72:73], v[218:219], v[218:219]
	v_mfma_f32_16x16x32_bf16 v[2:5], v[150:153], v[92:95], v[2:5]
	v_fma_f32 v78, v192, v192, v98
	v_fma_f32 v79, v193, v193, v98
	v_pk_fma_f32 v[98:99], v[200:201], v[200:201], v[126:127]
	v_pk_fma_f32 v[126:127], v[204:205], v[204:205], v[128:129] op_sel_hi:[1,1,0]
	v_mfma_f32_16x16x32_bf16 v[6:9], v[158:161], v[92:95], v[6:9]
	v_fma_f32 v128, v206, v206, v170
	v_fma_f32 v129, v207, v207, v170
	v_pk_fma_f32 v[134:135], v[212:213], v[212:213], v[176:177]
	v_pk_fma_f32 v[32:33], v[32:33], v[32:33], v[74:75] op_sel_hi:[1,1,0]
	v_pk_fma_f32 v[34:35], v[34:35], v[34:35], v[178:179] op_sel_hi:[1,1,0]
	v_pk_fma_f32 v[64:65], v[64:65], v[64:65], v[100:101] op_sel_hi:[1,1,0]
	v_pk_fma_f32 v[66:67], v[66:67], v[66:67], v[102:103] op_sel_hi:[1,1,0]
	v_pk_fma_f32 v[24:25], v[220:221], v[220:221], v[24:25]
	v_pk_fma_f32 v[26:27], v[26:27], v[26:27], v[60:61]
	v_pk_add_f32 v[28:29], v[28:29], v[30:31]
	v_mov_b32_e32 v69, v96
	v_mov_b32_e32 v71, v97
	v_lshlrev_b32_e32 v210, 16, v83
	v_mul_f32_e32 v174, v211, v211
	v_pk_fma_f32 v[130:131], v[208:209], v[208:209], v[172:173] op_sel_hi:[1,1,0]
	v_pk_fma_f32 v[72:73], v[216:217], v[216:217], v[72:73]
	v_mov_b32_e32 v77, v98
	v_mov_b32_e32 v127, v134
	v_mov_b32_e32 v129, v135
	v_mov_b32_e32 v33, v24
	v_mov_b32_e32 v35, v25
	v_mov_b32_e32 v65, v26
	v_mov_b32_e32 v67, v27
	v_pk_add_f32 v[24:25], v[36:37], v[28:29]
	v_pk_add_f32 v[26:27], v[68:69], v[70:71]
	v_pk_fma_f32 v[132:133], v[210:211], v[210:211], v[174:175] op_sel_hi:[1,1,0]
	v_mov_b32_e32 v79, v99
	v_mov_b32_e32 v131, v72
	v_pk_add_f32 v[28:29], v[126:127], v[128:129]
	v_pk_add_f32 v[24:25], v[62:63], v[24:25]
	v_pk_add_f32 v[26:27], v[76:77], v[26:27]
	v_mov_b32_e32 v133, v73
	v_mfma_f32_16x16x32_bf16 v[10:13], v[154:157], v[88:91], v[10:13]
	v_add_f32_e64 v30, v32, v34
	v_add_f32_e64 v31, v33, v35
	v_pk_add_f32 v[28:29], v[130:131], v[28:29]
	v_pk_add_f32 v[22:23], v[22:23], v[24:25]
	s_waitcnt vmcnt(0)
	v_mfma_f32_16x16x32_bf16 v[14:17], v[162:165], v[88:91], v[14:17]
	v_add_f32_e64 v24, v78, v26
	v_add_f32_e64 v25, v79, v27
	v_pk_add_f32 v[30:31], v[64:65], v[30:31]
	v_pk_add_f32 v[26:27], v[132:133], v[28:29]
	v_mfma_f32_16x16x32_bf16 v[2:5], v[154:157], v[92:95], v[2:5]
	v_add_f32_e64 v22, v22, v24
	v_add_f32_e64 v23, v23, v25
	v_pk_add_f32 v[28:29], v[66:67], v[30:31]
	v_pk_add_f32 v[22:23], v[22:23], v[26:27]
	v_mfma_f32_16x16x32_bf16 v[6:9], v[162:165], v[92:95], v[6:9]
	v_add_f32_e64 v22, v22, v28
	v_add_f32_e64 v23, v23, v29
	s_cbranch_scc0 .LBB0_817
	ds_bpermute_b32 v18, v105, v22
	s_waitcnt lgkmcnt(0)
	v_add_f32_e32 v18, v22, v18
	ds_bpermute_b32 v19, v106, v18
	s_and_saveexec_b64 s[8:9], s[2:3]
	s_cbranch_execz .LBB0_820
	s_waitcnt lgkmcnt(0)
	v_add_f32_e32 v18, v18, v19
	ds_write_b32 v121, v18 offset:32768
